# code placement: 64 bytes of padding before the attention main-loop head (shifts attention loop and later phases); no instruction changes otherwise
# baseline (speedup 1.0000x reference)
.LBB0_1127:
	s_mul_i32 s4, s9, 0x88000
	s_mul_hi_u32 s2, s8, 0x88000
	v_mov_b32_e32 v165, v0
	s_add_i32 s3, s2, s4
	s_mul_i32 s2, s8, 0x88000
	v_readlane_b32 s18, v251, 60
	global_load_dword v177, v163, s[46:47]
	v_readlane_b32 s19, v251, 61
	s_waitcnt vmcnt(8)
	v_and_b32_e32 v175, 31, v165
	v_ashrrev_i32_e32 v199, 8, v165
	s_add_u32 s2, s18, s2
	s_mul_i32 s1, s1, 0x110000
	s_mul_hi_u32 s9, s0, 0x110000
	v_bfe_u32 v198, v165, 6, 2
	v_mul_hi_i32_i24_e32 v3, s24, v199
	v_mul_i32_i24_e32 v2, s24, v199
	v_lshlrev_b32_e32 v203, 7, v175
	s_addc_u32 s3, s19, s3
	s_add_i32 s9, s9, s1
	s_mul_i32 s18, s0, 0x110000
	v_readlane_b32 s50, v253, 15
	v_bfe_u32 v176, v165, 5, 1
	v_lshl_add_u64 v[2:3], v[2:3], 1, s[12:13]
	v_lshl_or_b32 v162, v198, 12, v203
	v_ashrrev_i32_e32 v18, 4, v165
	v_readlane_b32 s51, v253, 16
	s_add_u32 s18, s50, s18
	v_lshl_add_u64 v[2:3], v[2:3], 0, v[162:163]
	v_lshlrev_b32_e32 v162, 4, v176
	v_lshlrev_b32_e32 v24, 3, v165
	v_ashrrev_i32_e32 v19, 31, v18
	s_addc_u32 s19, s51, s9
	v_lshl_add_u64 v[2:3], v[2:3], 0, v[162:163]
	v_and_b32_e32 v4, 0x78, v24
	v_add_u32_e32 v20, 32, v18
	s_waitcnt vmcnt(5)
	v_lshlrev_b64 v[42:43], 8, v[18:19]
	global_load_dwordx4 v[126:129], v[2:3], off
	global_load_dwordx4 v[122:125], v[2:3], off offset:32
	global_load_dwordx4 v[118:121], v[2:3], off offset:64
	global_load_dwordx4 v[114:117], v[2:3], off offset:96
	v_lshl_add_u64 v[2:3], s[18:19], 0, v[42:43]
	v_lshlrev_b32_e32 v4, 1, v4
	v_mov_b32_e32 v5, v163
	v_ashrrev_i32_e32 v21, 31, v20
	v_lshl_add_u64 v[44:45], v[2:3], 0, v[4:5]
	v_lshlrev_b64 v[2:3], 8, v[20:21]
	v_lshl_add_u64 v[2:3], s[18:19], 0, v[2:3]
	v_ashrrev_i32_e32 v22, 3, v165
	v_lshl_add_u64 v[6:7], v[2:3], 0, v[4:5]
	v_lshlrev_b32_e32 v38, 4, v165
	s_barrier
	global_load_dwordx4 v[2:5], v[44:45], off
	s_nop 0
	global_load_dwordx4 v[6:9], v[6:7], off
	v_ashrrev_i32_e32 v23, 31, v22
	v_and_b32_e32 v25, 0x70, v38
	s_add_u32 s12, s2, 0x88000
	v_lshlrev_b64 v[46:47], 7, v[22:23]
	s_addc_u32 s13, s3, 0
	v_or_b32_e32 v48, v46, v25
	v_mov_b32_e32 v49, v47
	v_lshl_add_u64 v[10:11], s[2:3], 0, v[48:49]
	v_lshl_add_u64 v[14:15], s[12:13], 0, v[48:49]
	global_load_dwordx4 v[10:13], v[10:11], off
	s_nop 0
	global_load_dwordx4 v[14:17], v[14:15], off
	v_and_b32_e32 v19, 0xfffff0, v18
	v_lshlrev_b32_e32 v21, 1, v18
	v_and_or_b32 v19, v21, 8, v19
	v_lshrrev_b32_e32 v21, 1, v18
	v_lshrrev_b32_e32 v19, 1, v19
	v_bfe_u32 v23, v24, 5, 2
	v_and_b32_e32 v18, 3, v18
	v_or_b32_e32 v19, v19, v23
	v_and_or_b32 v18, v21, 4, v18
	v_lshlrev_b32_e32 v19, 9, v19
	v_lshlrev_b32_e32 v18, 6, v18
	v_and_b32_e32 v21, 48, v38
	v_or3_b32 v204, v19, v18, v21
	v_and_b32_e32 v19, 0xfffff0, v20
	v_lshlrev_b32_e32 v20, 1, v20
	v_and_or_b32 v19, v20, 8, v19
	v_lshrrev_b32_e32 v19, 1, v19
	v_or_b32_e32 v19, v19, v23
	v_lshlrev_b32_e32 v19, 9, v19
	v_or3_b32 v206, v19, v18, v21
	v_and_b32_e32 v18, -13, v22
	v_lshrrev_b32_e32 v20, 1, v22
	s_waitcnt vmcnt(11)
	v_add_u32_e32 v50, 0, v204
	v_lshlrev_b32_e32 v19, 1, v22
	v_and_or_b32 v18, v20, 4, v18
	v_and_b32_e32 v20, 4, v22
	s_waitcnt vmcnt(0)
	v_and_b32_e32 v53, 7, v165
	v_and_or_b32 v19, v19, 8, v18
	v_bitop3_b32 v18, v18, v20, 7 bitop3:0x6c
	v_lshlrev_b32_e32 v19, 7, v19
	v_lshlrev_b32_e32 v18, 4, v18
	v_lshl_add_u32 v207, v199, 13, 0
	v_bitop3_b32 v208, v18, v19, v25 bitop3:0xde
	v_add_u32_e32 v51, 0, v206
	v_add_u32_e32 v212, v207, v203
	v_add_u32_e32 v52, 0, v208
	s_movk_i32 s9, 0x60
	v_and_b32_e32 v200, 63, v165
	v_lshlrev_b32_e32 v54, 3, v200
	v_and_b32_e32 v55, 0xc0, v38
	s_mov_b64 s[18:19], 0x2000
	v_lshl_add_u64 v[34:35], v[48:49], 0, s[18:19]
	v_lshl_add_u64 v[30:31], s[2:3], 0, v[34:35]
	v_lshl_add_u64 v[34:35], s[12:13], 0, v[34:35]
	v_mov_b32_e32 v201, 0
	v_lshrrev_b32_sdwa v164, v191, v165 dst_sel:WORD_1 dst_unused:UNUSED_PAD src0_sel:DWORD src1_sel:DWORD
	s_mov_b32 s18, 0
	v_mov_b32_e32 v56, v201
	v_mov_b32_e32 v57, v201
	s_waitcnt vmcnt(9)
	v_mov_b32_e32 v58, v201
	v_mov_b32_e32 v59, v201
	v_mov_b32_e32 v60, v201
	v_mov_b32_e32 v61, v201
	v_mov_b32_e32 v62, v201
	v_mov_b32_e32 v63, v201
	v_mov_b32_e32 v64, v201
	v_mov_b32_e32 v65, v201
	s_waitcnt vmcnt(3)
	ds_write_b128 v50, v[2:5]
	v_lshrrev_b32_e32 v2, 1, v165
	v_bitop3_b32 v2, v2, v53, 4 bitop3:0x6c
	v_lshlrev_b32_e32 v39, 4, v2
	v_xor_b32_e32 v211, v39, v162
	s_waitcnt vmcnt(2)
	ds_write_b128 v51, v[6:9]
	v_add_u32_e32 v6, v212, v211
	s_waitcnt vmcnt(1)
	ds_write_b128 v52, v[10:13] offset:49152
	s_waitcnt vmcnt(0)
	ds_write_b128 v52, v[14:17] offset:57344
	s_waitcnt lgkmcnt(0)
	s_barrier
	ds_read_b128 v[2:5], v6 offset:49152
	ds_read_b128 v[18:21], v6 offset:53248
	s_waitcnt lgkmcnt(1)
	v_mfma_f32_32x32x16_bf16 v[2:17], v[2:5], v[126:129], 0
	v_bitop3_b32 v209, v162, v39, 32 bitop3:0x36
	v_add_u32_e32 v22, v212, v209
	v_bitop3_b32 v205, v162, v39, 64 bitop3:0x36
	v_bitop3_b32 v210, v162, v39, s9 bitop3:0x36
	v_add_u32_e32 v39, v212, v210
	s_mov_b32 s9, 1
	s_waitcnt lgkmcnt(0)
	v_mfma_f32_32x32x16_bf16 v[66:81], v[18:21], v[126:129], 0
	ds_read_b128 v[18:21], v22 offset:49152
	ds_read_b128 v[22:25], v22 offset:53248
	s_waitcnt lgkmcnt(1)
	v_mfma_f32_32x32x16_bf16 v[2:17], v[18:21], v[122:125], v[2:17]
	s_waitcnt lgkmcnt(0)
	v_mfma_f32_32x32x16_bf16 v[66:81], v[22:25], v[122:125], v[66:81]
	v_add_u32_e32 v22, v212, v205
	ds_read_b128 v[18:21], v22 offset:49152
	ds_read_b128 v[22:25], v22 offset:53248
	s_waitcnt lgkmcnt(1)
	v_mfma_f32_32x32x16_bf16 v[2:17], v[18:21], v[118:121], v[2:17]
	v_add_co_u32_e32 v18, vcc, s83, v44
	s_nop 1
	v_addc_co_u32_e32 v19, vcc, 0, v45, vcc
	v_add_co_u32_e32 v26, vcc, s77, v44
	s_waitcnt lgkmcnt(0)
	v_mfma_f32_32x32x16_bf16 v[66:81], v[22:25], v[118:121], v[66:81]
	v_addc_co_u32_e32 v27, vcc, 0, v45, vcc
	global_load_dwordx4 v[18:21], v[18:19], off
	s_nop 0
	global_load_dwordx4 v[26:29], v[26:27], off
	ds_read_b128 v[22:25], v39 offset:49152
	global_load_dwordx4 v[30:33], v[30:31], off
	ds_read_b128 v[38:41], v39 offset:53248
	global_load_dwordx4 v[34:37], v[34:35], off
	s_waitcnt lgkmcnt(1)
	v_mfma_f32_32x32x16_bf16 v[2:17], v[22:25], v[114:117], v[2:17]
	v_lshlrev_b32_e32 v23, 1, v165
	v_and_or_b32 v22, v54, 24, v55
	v_and_b32_e32 v23, 32, v23
	v_and_b32_e32 v24, 0x100, v54
	v_or3_b32 v22, v22, v23, v24
	v_add_u32_e32 v202, 0, v22
	v_lshl_add_u64 v[22:23], v[48:49], 0, s[36:37]
	v_lshl_add_u64 v[24:25], s[12:13], 0, v[22:23]
	v_lshl_add_u64 v[22:23], s[2:3], 0, v[22:23]
	global_load_dwordx4 v[142:145], v[24:25], off
	global_load_dwordx4 v[138:141], v[22:23], off
	v_add_co_u32_e32 v22, vcc, s79, v44
	s_waitcnt lgkmcnt(0)
	v_mfma_f32_32x32x16_bf16 v[66:81], v[38:41], v[114:117], v[66:81]
	v_addc_co_u32_e32 v23, vcc, 0, v45, vcc
	v_add_co_u32_e32 v24, vcc, s90, v44
	v_exp_f32_e32 v222, v2
	s_nop 0
	v_addc_co_u32_e32 v25, vcc, 0, v45, vcc
	global_load_dwordx4 v[134:137], v[22:23], off
	global_load_dwordx4 v[130:133], v[24:25], off
	v_exp_f32_e32 v225, v3
	v_exp_f32_e32 v219, v4
	v_exp_f32_e32 v223, v5
	v_exp_f32_e32 v218, v6
	v_exp_f32_e32 v220, v7
	v_exp_f32_e32 v221, v8
	v_exp_f32_e32 v224, v9
	v_exp_f32_e32 v173, v10
	v_exp_f32_e32 v216, v11
	v_exp_f32_e32 v171, v12
	v_exp_f32_e32 v214, v13
	v_exp_f32_e32 v170, v14
	v_exp_f32_e32 v217, v15
	v_exp_f32_e32 v172, v16
	v_exp_f32_e32 v215, v17
	v_mad_u64_u32 v[2:3], s[2:3], s8, v192, v[46:47]
	s_waitcnt vmcnt(4)
	s_waitcnt vmcnt(7)
	ds_write_b128 v50, v[18:21] offset:16384
	s_waitcnt vmcnt(6)
	ds_write_b128 v51, v[26:29] offset:16384
	v_add_u32_e32 v18, 0x10000, v52
	v_add_u32_e32 v167, s4, v3
	v_lshl_or_b32 v166, v53, 4, v2
	v_mad_u64_u32 v[2:3], s[2:3], s0, v193, v[42:43]
	s_waitcnt vmcnt(5)
	ds_write_b128 v18, v[30:33]
	v_add_u32_e32 v18, 0x12000, v52
	v_add_u32_e32 v169, s1, v3
	v_and_b32_e32 v3, 15, v165
	s_waitcnt vmcnt(4)
	ds_write_b128 v18, v[34:37]
	v_lshl_or_b32 v168, v3, 4, v2
	s_mov_b32 s0, 2
	v_mov_b32_e32 v50, 0
	v_mov_b32_e32 v51, v201
	v_mov_b32_e32 v52, v201
	v_mov_b32_e32 v53, v201
	v_mov_b32_e32 v54, v201
	v_mov_b32_e32 v55, v201
	v_mov_b32_e32 v34, 0
	v_mov_b32_e32 v35, v201
	v_mov_b32_e32 v36, v201
	v_mov_b32_e32 v37, v201
	v_mov_b32_e32 v38, v201
	v_mov_b32_e32 v39, v201
	v_mov_b32_e32 v40, v201
	v_mov_b32_e32 v41, v201
	v_mov_b32_e32 v42, v201
	v_mov_b32_e32 v43, v201
	v_mov_b32_e32 v44, v201
	v_mov_b32_e32 v45, v201
	v_mov_b32_e32 v46, v201
	v_mov_b32_e32 v47, v201
	v_mov_b32_e32 v48, v201
	v_mov_b32_e32 v49, v201
	v_mov_b32_e32 v18, 0
	v_mov_b32_e32 v19, v201
	v_mov_b32_e32 v20, v201
	v_mov_b32_e32 v21, v201
	v_mov_b32_e32 v22, v201
	v_mov_b32_e32 v23, v201
	v_mov_b32_e32 v24, v201
	v_mov_b32_e32 v25, v201
	v_mov_b32_e32 v26, v201
	v_mov_b32_e32 v27, v201
	v_mov_b32_e32 v28, v201
	v_mov_b32_e32 v29, v201
	v_mov_b32_e32 v30, v201
	v_mov_b32_e32 v31, v201
	v_mov_b32_e32 v32, v201
	v_mov_b32_e32 v33, v201
	v_mov_b32_e32 v2, 0
	v_mov_b32_e32 v3, v201
	v_mov_b32_e32 v4, v201
	v_mov_b32_e32 v5, v201
	v_mov_b32_e32 v6, v201
	v_mov_b32_e32 v7, v201
	v_mov_b32_e32 v8, v201
	v_mov_b32_e32 v9, v201
	v_mov_b32_e32 v10, v201
	v_mov_b32_e32 v11, v201
	v_mov_b32_e32 v12, v201
	v_mov_b32_e32 v13, v201
	v_mov_b32_e32 v14, v201
	v_mov_b32_e32 v15, v201
	v_mov_b32_e32 v16, v201
	v_mov_b32_e32 v17, v201
	s_waitcnt lgkmcnt(0)
	s_barrier
	s_nop 0
	s_nop 0
	s_nop 0
	s_nop 0
	s_nop 0
	s_nop 0
	s_nop 0
	s_nop 0
	s_nop 0
	s_nop 0
	s_nop 0
	s_nop 0
	s_nop 0
	s_nop 0
	s_nop 0
	s_nop 0
